# lasthalf
# speedup vs baseline: 1.0124x; 1.0049x over previous
.LBB0_34:
	s_or_b64 exec, exec, s[10:11]
	ds_read_b128 v[18:21], v72
	s_waitcnt vmcnt(2)
	v_cvt_pk_f16_f32 v14, v14, v15
	v_cvt_pk_f16_f32 v15, v16, v17
	v_cvt_pk_f16_f32 v16, v10, v11
	ds_read_b128 v[22:25], v71 offset:41984
	v_cvt_pk_f16_f32 v17, v12, v13
	ds_read_b128 v[10:13], v72 offset:1024
	ds_read_b128 v[26:29], v71 offset:42048
	s_waitcnt vmcnt(0)
	v_cvt_pk_f16_f32 v0, v6, v7
	v_cvt_pk_f16_f32 v1, v8, v9
	v_cvt_pk_f16_f32 v2, v2, v3
	v_cvt_pk_f16_f32 v3, v4, v5
	s_waitcnt lgkmcnt(2)
	v_mfma_f32_16x16x32_f16 v[30:33], v[18:21], v[14:17], v[22:25]
	s_add_i32 s10, s20, s12
	v_mfma_f32_16x16x32_f16 v[18:21], v[18:21], v[0:3], v[22:25]
	ds_read_b128 v[4:7], v72 offset:2048
	s_nop 1
	ds_read_b128 v[22:25], v71 offset:42112
	s_waitcnt lgkmcnt(2)
	v_mfma_f32_16x16x32_f16 v[34:37], v[10:13], v[14:17], v[26:29]
	v_exp_f32_e32 v78, v30
	v_exp_f32_e32 v79, v31
	v_exp_f32_e32 v20, v20
	v_mfma_f32_16x16x32_f16 v[8:11], v[10:13], v[0:3], v[26:29]
	ds_read_b128 v[44:47], v71 offset:42176
	s_nop 2
	v_exp_f32_e64 v80, v34 clamp
	v_exp_f32_e64 v81, v35 clamp
	ds_read_b128 v[26:29], v72 offset:3072
	s_waitcnt lgkmcnt(2)
	v_mfma_f32_16x16x32_f16 v[48:51], v[4:7], v[14:17], v[22:25]
	v_exp_f32_e64 v82, v36 clamp
	v_exp_f32_e64 v83, v37 clamp
	v_exp_f32_e32 v21, v21
	v_mfma_f32_16x16x32_f16 v[22:25], v[4:7], v[0:3], v[22:25]
	ds_read_b128 v[52:55], v72 offset:4096
	ds_read_b128 v[56:59], v71 offset:42240
	s_nop 1
	v_exp_f32_e32 v4, v48
	s_waitcnt lgkmcnt(2)
	v_mfma_f32_16x16x32_f16 v[60:63], v[26:29], v[14:17], v[44:47]
	v_exp_f32_e32 v5, v49
	v_exp_f32_e32 v48, v32
	v_exp_f32_e32 v49, v33
	v_mfma_f32_16x16x32_f16 v[26:29], v[26:29], v[0:3], v[44:47]
	ds_read_b128 v[64:67], v71 offset:42304
	v_exp_f32_e32 v6, v50
	v_exp_f32_e32 v7, v51
	ds_read_b128 v[44:47], v72 offset:5120
	s_waitcnt lgkmcnt(2)
	v_mfma_f32_16x16x32_f16 v[74:77], v[52:55], v[14:17], v[56:59]
	v_exp_f32_e32 v50, v18
	v_exp_f32_e32 v51, v19
	v_exp_f32_e32 v26, v26
	v_mfma_f32_16x16x32_f16 v[30:33], v[52:55], v[0:3], v[56:59]
	v_exp_f32_e64 v52, v8 clamp
	v_exp_f32_e64 v53, v9 clamp
	v_exp_f32_e32 v8, v22
	s_waitcnt lgkmcnt(0)
	v_mfma_f32_16x16x32_f16 v[34:37], v[44:47], v[14:17], v[64:67]
	v_exp_f32_e32 v9, v23
	v_exp_f32_e64 v22, v10 clamp
	v_exp_f32_e64 v23, v11 clamp
	v_mfma_f32_16x16x32_f16 v[44:47], v[44:47], v[0:3], v[64:67]
	v_exp_f32_e32 v10, v24
	v_exp_f32_e32 v11, v25
	s_nop 1
	v_exp_f32_e32 v12, v34
	v_exp_f32_e32 v13, v35
	v_exp_f32_e32 v18, v36
	v_exp_f32_e32 v24, v60
	v_exp_f32_e32 v25, v61
	v_exp_f32_e64 v54, v74 clamp
	v_exp_f32_e64 v55, v75 clamp
	v_exp_f32_e32 v34, v62
	v_exp_f32_e32 v35, v63
	v_exp_f32_e64 v56, v76 clamp
	v_exp_f32_e64 v57, v77 clamp
	v_exp_f32_e32 v19, v37
	v_exp_f32_e32 v27, v27
	v_exp_f32_e64 v30, v30 clamp
	v_exp_f32_e64 v31, v31 clamp
	v_exp_f32_e32 v36, v44
	v_exp_f32_e32 v37, v45
	v_exp_f32_e32 v28, v28
	v_exp_f32_e32 v29, v29
	v_exp_f32_e64 v32, v32 clamp
	v_exp_f32_e64 v33, v33 clamp
	v_exp_f32_e32 v44, v46
	v_exp_f32_e32 v45, v47
	v_pk_fma_f32 v[58:59], v[80:81], s[2:3], 1.0 op_sel_hi:[1,0,0]
	v_pk_fma_f32 v[60:61], v[82:83], s[2:3], 1.0 op_sel_hi:[1,0,0]
	v_pk_fma_f32 v[52:53], v[52:53], s[2:3], 1.0 op_sel_hi:[1,0,0]
	v_pk_fma_f32 v[22:23], v[22:23], s[2:3], 1.0 op_sel_hi:[1,0,0]
	v_pk_fma_f32 v[54:55], v[54:55], s[2:3], 1.0 op_sel_hi:[1,0,0]
	v_pk_fma_f32 v[56:57], v[56:57], s[2:3], 1.0 op_sel_hi:[1,0,0]
	v_pk_fma_f32 v[30:31], v[30:31], s[2:3], 1.0 op_sel_hi:[1,0,0]
	v_pk_fma_f32 v[32:33], v[32:33], s[2:3], 1.0 op_sel_hi:[1,0,0]
	v_pk_fma_f32 v[46:47], v[78:79], v[58:59], v[58:59]
	v_pk_fma_f32 v[48:49], v[48:49], v[60:61], v[60:61]
	v_pk_fma_f32 v[50:51], v[50:51], v[52:53], v[52:53]
	v_pk_fma_f32 v[20:21], v[20:21], v[22:23], v[22:23]
	v_pk_fma_f32 v[24:25], v[24:25], v[54:55], v[54:55]
	v_pk_fma_f32 v[34:35], v[34:35], v[56:57], v[56:57]
	v_pk_fma_f32 v[26:27], v[26:27], v[30:31], v[30:31]
	v_pk_fma_f32 v[28:29], v[28:29], v[32:33], v[32:33]
	v_pk_fma_f32 v[58:59], v[58:59], s[6:7], v[40:41] op_sel_hi:[1,0,0] neg_lo:[1,0,0] neg_hi:[1,0,0]
	v_pk_fma_f32 v[60:61], v[60:61], s[6:7], v[40:41] op_sel_hi:[1,0,0] neg_lo:[1,0,0] neg_hi:[1,0,0]
	v_pk_fma_f32 v[52:53], v[52:53], s[6:7], v[40:41] op_sel_hi:[1,0,0] neg_lo:[1,0,0] neg_hi:[1,0,0]
	v_pk_fma_f32 v[22:23], v[22:23], s[6:7], v[40:41] op_sel_hi:[1,0,0] neg_lo:[1,0,0] neg_hi:[1,0,0]
	v_pk_fma_f32 v[54:55], v[54:55], s[6:7], v[40:41] op_sel_hi:[1,0,0] neg_lo:[1,0,0] neg_hi:[1,0,0]
	v_pk_fma_f32 v[56:57], v[56:57], s[6:7], v[40:41] op_sel_hi:[1,0,0] neg_lo:[1,0,0] neg_hi:[1,0,0]
	v_pk_fma_f32 v[30:31], v[30:31], s[6:7], v[40:41] op_sel_hi:[1,0,0] neg_lo:[1,0,0] neg_hi:[1,0,0]
	v_pk_fma_f32 v[32:33], v[32:33], s[6:7], v[40:41] op_sel_hi:[1,0,0] neg_lo:[1,0,0] neg_hi:[1,0,0]
	v_pk_fma_f32 v[46:47], v[4:5], v[46:47], v[46:47]
	v_pk_fma_f32 v[48:49], v[6:7], v[48:49], v[48:49]
	v_pk_fma_f32 v[50:51], v[8:9], v[50:51], v[50:51]
	v_pk_fma_f32 v[20:21], v[10:11], v[20:21], v[20:21]
	v_pk_fma_f32 v[24:25], v[12:13], v[24:25], v[24:25]
	v_pk_fma_f32 v[34:35], v[18:19], v[34:35], v[34:35]
	v_pk_fma_f32 v[26:27], v[36:37], v[26:27], v[26:27]
	v_pk_fma_f32 v[28:29], v[44:45], v[28:29], v[28:29]
	v_rcp_f32_e64 v46, v46 clamp
	v_rcp_f32_e64 v47, v47 clamp
	v_rcp_f32_e64 v48, v48 clamp
	v_rcp_f32_e64 v49, v49 clamp
	v_rcp_f32_e64 v50, v50 clamp
	v_rcp_f32_e64 v51, v51 clamp
	v_rcp_f32_e64 v20, v20 clamp
	v_rcp_f32_e64 v21, v21 clamp
	v_rcp_f32_e64 v24, v24 clamp
	v_rcp_f32_e64 v25, v25 clamp
	v_rcp_f32_e64 v34, v34 clamp
	v_rcp_f32_e64 v35, v35 clamp
	v_rcp_f32_e64 v26, v26 clamp
	v_rcp_f32_e64 v27, v27 clamp
	v_rcp_f32_e64 v28, v28 clamp
	v_rcp_f32_e64 v29, v29 clamp
	v_pk_mul_f32 v[46:47], v[58:59], v[46:47]
	v_pk_mul_f32 v[48:49], v[60:61], v[48:49]
	v_pk_mul_f32 v[50:51], v[52:53], v[50:51]
	v_pk_mul_f32 v[20:21], v[22:23], v[20:21]
	v_pk_mul_f32 v[22:23], v[54:55], v[24:25]
	v_pk_mul_f32 v[24:25], v[56:57], v[34:35]
	v_pk_mul_f32 v[26:27], v[30:31], v[26:27]
	v_pk_mul_f32 v[28:29], v[32:33], v[28:29]
	v_pk_fma_f32 v[4:5], v[4:5], v[46:47], v[46:47]
	v_pk_fma_f32 v[6:7], v[6:7], v[48:49], v[48:49]
	v_pk_fma_f32 v[8:9], v[8:9], v[50:51], v[50:51]
	v_pk_fma_f32 v[10:11], v[10:11], v[20:21], v[20:21]
	v_pk_fma_f32 v[12:13], v[12:13], v[22:23], v[22:23]
	v_pk_fma_f32 v[18:19], v[18:19], v[24:25], v[24:25]
	v_pk_fma_f32 v[30:31], v[36:37], v[26:27], v[26:27]
	v_pk_fma_f32 v[32:33], v[44:45], v[28:29], v[28:29]
	s_nop 0
	v_pk_fma_f32 v[4:5], v[4:5], v[4:5], s[4:5] neg_lo:[1,0,0] neg_hi:[1,0,0] clamp
	v_pk_fma_f32 v[6:7], v[6:7], v[6:7], s[4:5] neg_lo:[1,0,0] neg_hi:[1,0,0] clamp
	v_pk_fma_f32 v[8:9], v[8:9], v[8:9], s[4:5] neg_lo:[1,0,0] neg_hi:[1,0,0] clamp
	v_pk_fma_f32 v[10:11], v[10:11], v[10:11], s[4:5] neg_lo:[1,0,0] neg_hi:[1,0,0] clamp
	v_pk_fma_f32 v[12:13], v[12:13], v[12:13], s[4:5] neg_lo:[1,0,0] neg_hi:[1,0,0] clamp
	v_pk_fma_f32 v[18:19], v[18:19], v[18:19], s[4:5] neg_lo:[1,0,0] neg_hi:[1,0,0] clamp
	v_pk_fma_f32 v[30:31], v[30:31], v[30:31], s[4:5] neg_lo:[1,0,0] neg_hi:[1,0,0] clamp
	s_nop 0
	v_pk_fma_f32 v[32:33], v[32:33], v[32:33], s[4:5] neg_lo:[1,0,0] neg_hi:[1,0,0] clamp
	s_nop 0
	v_pk_fma_f32 v[8:9], v[8:9], v[8:9], s[8:9] op_sel_hi:[1,1,0]
	v_pk_fma_f32 v[10:11], v[10:11], v[10:11], s[8:9] op_sel_hi:[1,1,0]
	v_pk_fma_f32 v[12:13], v[12:13], v[12:13], s[8:9] op_sel_hi:[1,1,0]
	v_pk_fma_f32 v[18:19], v[18:19], v[18:19], s[8:9] op_sel_hi:[1,1,0]
	v_pk_fma_f32 v[32:33], v[32:33], v[32:33], s[8:9] op_sel_hi:[1,1,0]
	v_pk_fma_f32 v[4:5], v[4:5], v[4:5], s[8:9] op_sel_hi:[1,1,0]
	v_pk_fma_f32 v[6:7], v[6:7], v[6:7], s[8:9] op_sel_hi:[1,1,0]
	v_pk_fma_f32 v[30:31], v[30:31], v[30:31], s[8:9] op_sel_hi:[1,1,0]
	v_pk_mul_f32 v[8:9], v[50:51], v[8:9]
	v_pk_mul_f32 v[84:85], v[20:21], v[10:11]
	v_pk_mul_f32 v[86:87], v[22:23], v[12:13]
	v_pk_mul_f32 v[10:11], v[24:25], v[18:19]
	v_pk_mul_f32 v[12:13], v[28:29], v[32:33]
	v_pk_mul_f32 v[64:65], v[46:47], v[4:5]
	v_pk_mul_f32 v[82:83], v[48:49], v[6:7]
	v_pk_mul_f32 v[20:21], v[30:31], v[26:27]
	ds_read_b128 v[4:7], v72 offset:6144
	ds_read_b128 v[22:25], v71 offset:42368
	ds_read_b128 v[26:29], v72 offset:7168
	ds_read_b128 v[30:33], v71 offset:42432
	v_cvt_pk_f16_f32 v19, v84, v85
	v_cvt_pk_f16_f32 v18, v8, v9
	v_cvt_pk_f16_f32 v20, v20, v21
	v_cvt_pk_f16_f32 v21, v12, v13
	s_waitcnt lgkmcnt(2)
	v_mfma_f32_16x16x32_f16 v[34:37], v[4:7], v[14:17], v[22:25]
	v_mfma_f32_16x16x32_f16 v[44:47], v[4:7], v[0:3], v[22:25]
	ds_read_b128 v[4:7], v72 offset:8192
	ds_read_b128 v[48:51], v71 offset:42496
	s_waitcnt lgkmcnt(2)
	v_mfma_f32_16x16x32_f16 v[52:55], v[26:29], v[14:17], v[30:33]
	v_cvt_pk_f16_f32 v22, v64, v65
	v_cvt_pk_f16_f32 v23, v82, v83
	v_cvt_pk_f16_f32 v24, v86, v87
	v_mfma_f32_16x16x32_f16 v[26:29], v[26:29], v[0:3], v[30:33]
	ds_read_b128 v[56:59], v71 offset:42560
	v_exp_f32_e32 v86, v34
	v_exp_f32_e32 v87, v35
	ds_read_b128 v[30:33], v72 offset:9216
	s_waitcnt lgkmcnt(2)
	v_mfma_f32_16x16x32_f16 v[60:63], v[4:7], v[14:17], v[48:51]
	v_exp_f32_e64 v88, v52 clamp
	v_exp_f32_e64 v89, v53 clamp
	v_exp_f32_e64 v90, v54 clamp
	v_mfma_f32_16x16x32_f16 v[48:51], v[4:7], v[0:3], v[48:51]
	ds_read_b128 v[64:67], v72 offset:10240
	ds_read_b128 v[74:77], v71 offset:42624
	s_nop 1
	v_exp_f32_e32 v4, v60
	s_waitcnt lgkmcnt(2)
	v_mfma_f32_16x16x32_f16 v[78:81], v[30:33], v[14:17], v[56:59]
	v_exp_f32_e32 v5, v61
	v_exp_f32_e32 v60, v36
	v_exp_f32_e32 v61, v37
	v_mfma_f32_16x16x32_f16 v[30:33], v[30:33], v[0:3], v[56:59]
	ds_read_b128 v[82:85], v71 offset:42688
	v_exp_f32_e64 v91, v55 clamp
	v_exp_f32_e32 v6, v62
	ds_read_b128 v[56:59], v72 offset:11264
	s_waitcnt lgkmcnt(2)
	v_mfma_f32_16x16x32_f16 v[34:37], v[64:67], v[14:17], v[74:77]
	v_exp_f32_e32 v7, v63
	v_exp_f32_e32 v8, v48
	v_exp_f32_e32 v9, v49
	v_mfma_f32_16x16x32_f16 v[52:55], v[64:67], v[0:3], v[74:77]
	v_exp_f32_e32 v44, v44
	v_exp_f32_e32 v45, v45
	v_exp_f32_e64 v26, v26 clamp
	s_waitcnt lgkmcnt(0)
	v_mfma_f32_16x16x32_f16 v[14:17], v[56:59], v[14:17], v[82:85]
	v_exp_f32_e64 v27, v27 clamp
	v_exp_f32_e32 v46, v46
	v_exp_f32_e32 v47, v47
	v_mfma_f32_16x16x32_f16 v[56:59], v[56:59], v[0:3], v[82:85]
	v_exp_f32_e64 v28, v28 clamp
	s_nop 2
	v_exp_f32_e32 v2, v14
	v_exp_f32_e32 v3, v15
	v_exp_f32_e32 v14, v16
	v_exp_f32_e32 v15, v17
	v_exp_f32_e32 v16, v30
	v_exp_f32_e32 v17, v31
	v_exp_f32_e64 v29, v29 clamp
	v_exp_f32_e32 v0, v50
	v_exp_f32_e32 v1, v51
	v_exp_f32_e32 v48, v78
	v_exp_f32_e32 v49, v79
	v_exp_f32_e64 v34, v34 clamp
	v_exp_f32_e64 v35, v35 clamp
	v_exp_f32_e32 v50, v80
	v_exp_f32_e32 v51, v81
	v_exp_f32_e64 v36, v36 clamp
	v_exp_f32_e64 v37, v37 clamp
	v_exp_f32_e64 v30, v52 clamp
	v_exp_f32_e64 v31, v53 clamp
	v_exp_f32_e32 v52, v56
	v_exp_f32_e32 v53, v57
	v_exp_f32_e32 v32, v32
	v_exp_f32_e32 v33, v33
	v_exp_f32_e64 v54, v54 clamp
	v_exp_f32_e64 v55, v55 clamp
	v_exp_f32_e32 v56, v58
	v_cvt_pk_f16_f32 v25, v10, v11
	v_exp_f32_e32 v57, v59
	v_pk_fma_f32 v[30:31], v[30:31], s[2:3], 1.0 op_sel_hi:[1,0,0]
	v_pk_fma_f32 v[10:11], v[88:89], s[2:3], 1.0 op_sel_hi:[1,0,0]
	v_pk_fma_f32 v[12:13], v[90:91], s[2:3], 1.0 op_sel_hi:[1,0,0]
	v_pk_fma_f32 v[26:27], v[26:27], s[2:3], 1.0 op_sel_hi:[1,0,0]
	v_pk_fma_f32 v[28:29], v[28:29], s[2:3], 1.0 op_sel_hi:[1,0,0]
	v_pk_fma_f32 v[34:35], v[34:35], s[2:3], 1.0 op_sel_hi:[1,0,0]
	v_pk_fma_f32 v[36:37], v[36:37], s[2:3], 1.0 op_sel_hi:[1,0,0]
	v_pk_fma_f32 v[54:55], v[54:55], s[2:3], 1.0 op_sel_hi:[1,0,0]
	v_pk_fma_f32 v[16:17], v[16:17], v[30:31], v[30:31]
	v_pk_fma_f32 v[58:59], v[86:87], v[10:11], v[10:11]
	v_pk_fma_f32 v[10:11], v[10:11], s[6:7], v[40:41] op_sel_hi:[1,0,0] neg_lo:[1,0,0] neg_hi:[1,0,0]
	v_pk_fma_f32 v[60:61], v[60:61], v[12:13], v[12:13]
	v_pk_fma_f32 v[12:13], v[12:13], s[6:7], v[40:41] op_sel_hi:[1,0,0] neg_lo:[1,0,0] neg_hi:[1,0,0]
	v_pk_fma_f32 v[44:45], v[44:45], v[26:27], v[26:27]
	v_pk_fma_f32 v[46:47], v[46:47], v[28:29], v[28:29]
	v_pk_fma_f32 v[48:49], v[48:49], v[34:35], v[34:35]
	v_pk_fma_f32 v[50:51], v[50:51], v[36:37], v[36:37]
	v_pk_fma_f32 v[32:33], v[32:33], v[54:55], v[54:55]
	v_pk_fma_f32 v[16:17], v[52:53], v[16:17], v[16:17]
	v_pk_fma_f32 v[26:27], v[26:27], s[6:7], v[40:41] op_sel_hi:[1,0,0] neg_lo:[1,0,0] neg_hi:[1,0,0]
	v_pk_fma_f32 v[28:29], v[28:29], s[6:7], v[40:41] op_sel_hi:[1,0,0] neg_lo:[1,0,0] neg_hi:[1,0,0]
	v_pk_fma_f32 v[34:35], v[34:35], s[6:7], v[40:41] op_sel_hi:[1,0,0] neg_lo:[1,0,0] neg_hi:[1,0,0]
	v_pk_fma_f32 v[36:37], v[36:37], s[6:7], v[40:41] op_sel_hi:[1,0,0] neg_lo:[1,0,0] neg_hi:[1,0,0]
	v_pk_fma_f32 v[30:31], v[30:31], s[6:7], v[40:41] op_sel_hi:[1,0,0] neg_lo:[1,0,0] neg_hi:[1,0,0]
	v_pk_fma_f32 v[54:55], v[54:55], s[6:7], v[40:41] op_sel_hi:[1,0,0] neg_lo:[1,0,0] neg_hi:[1,0,0]
	v_pk_fma_f32 v[58:59], v[4:5], v[58:59], v[58:59]
	v_pk_fma_f32 v[60:61], v[6:7], v[60:61], v[60:61]
	v_pk_fma_f32 v[44:45], v[8:9], v[44:45], v[44:45]
	v_pk_fma_f32 v[46:47], v[0:1], v[46:47], v[46:47]
	v_pk_fma_f32 v[48:49], v[2:3], v[48:49], v[48:49]
	v_pk_fma_f32 v[50:51], v[14:15], v[50:51], v[50:51]
	v_pk_fma_f32 v[32:33], v[56:57], v[32:33], v[32:33]
	v_rcp_f32_e64 v16, v16 clamp
	v_rcp_f32_e64 v17, v17 clamp
	v_rcp_f32_e64 v58, v58 clamp
	v_rcp_f32_e64 v59, v59 clamp
	v_rcp_f32_e64 v60, v60 clamp
	v_rcp_f32_e64 v61, v61 clamp
	v_rcp_f32_e64 v44, v44 clamp
	v_rcp_f32_e64 v45, v45 clamp
	v_rcp_f32_e64 v46, v46 clamp
	v_rcp_f32_e64 v47, v47 clamp
	v_rcp_f32_e64 v48, v48 clamp
	v_rcp_f32_e64 v49, v49 clamp
	v_rcp_f32_e64 v50, v50 clamp
	v_rcp_f32_e64 v51, v51 clamp
	v_rcp_f32_e64 v32, v32 clamp
	v_rcp_f32_e64 v33, v33 clamp
	v_pk_mul_f32 v[10:11], v[10:11], v[58:59]
	v_pk_mul_f32 v[12:13], v[12:13], v[60:61]
	v_pk_mul_f32 v[26:27], v[26:27], v[44:45]
	v_pk_mul_f32 v[34:35], v[34:35], v[48:49]
	v_pk_mul_f32 v[36:37], v[36:37], v[50:51]
	v_pk_mul_f32 v[28:29], v[28:29], v[46:47]
	v_pk_mul_f32 v[16:17], v[30:31], v[16:17]
	v_pk_mul_f32 v[30:31], v[54:55], v[32:33]
	v_pk_fma_f32 v[4:5], v[4:5], v[10:11], v[10:11]
	v_pk_fma_f32 v[6:7], v[6:7], v[12:13], v[12:13]
	v_pk_fma_f32 v[8:9], v[8:9], v[26:27], v[26:27]
	v_pk_fma_f32 v[2:3], v[2:3], v[34:35], v[34:35]
	v_pk_fma_f32 v[14:15], v[14:15], v[36:37], v[36:37]
	v_pk_fma_f32 v[0:1], v[0:1], v[28:29], v[28:29]
	v_pk_fma_f32 v[32:33], v[52:53], v[16:17], v[16:17]
	v_pk_fma_f32 v[44:45], v[56:57], v[30:31], v[30:31]
	s_nop 0
	v_pk_fma_f32 v[4:5], v[4:5], v[4:5], s[4:5] neg_lo:[1,0,0] neg_hi:[1,0,0] clamp
	v_pk_fma_f32 v[6:7], v[6:7], v[6:7], s[4:5] neg_lo:[1,0,0] neg_hi:[1,0,0] clamp
	v_pk_fma_f32 v[8:9], v[8:9], v[8:9], s[4:5] neg_lo:[1,0,0] neg_hi:[1,0,0] clamp
	v_pk_fma_f32 v[0:1], v[0:1], v[0:1], s[4:5] neg_lo:[1,0,0] neg_hi:[1,0,0] clamp
	v_pk_fma_f32 v[2:3], v[2:3], v[2:3], s[4:5] neg_lo:[1,0,0] neg_hi:[1,0,0] clamp
	v_pk_fma_f32 v[14:15], v[14:15], v[14:15], s[4:5] neg_lo:[1,0,0] neg_hi:[1,0,0] clamp
	v_pk_fma_f32 v[32:33], v[32:33], v[32:33], s[4:5] neg_lo:[1,0,0] neg_hi:[1,0,0] clamp
	s_nop 0
	v_pk_fma_f32 v[44:45], v[44:45], v[44:45], s[4:5] neg_lo:[1,0,0] neg_hi:[1,0,0] clamp
	s_nop 0
	v_pk_fma_f32 v[32:33], v[32:33], v[32:33], s[8:9] op_sel_hi:[1,1,0]
	v_pk_fma_f32 v[4:5], v[4:5], v[4:5], s[8:9] op_sel_hi:[1,1,0]
	v_pk_fma_f32 v[6:7], v[6:7], v[6:7], s[8:9] op_sel_hi:[1,1,0]
	v_pk_fma_f32 v[8:9], v[8:9], v[8:9], s[8:9] op_sel_hi:[1,1,0]
	v_pk_fma_f32 v[0:1], v[0:1], v[0:1], s[8:9] op_sel_hi:[1,1,0]
	v_pk_fma_f32 v[2:3], v[2:3], v[2:3], s[8:9] op_sel_hi:[1,1,0]
	v_pk_fma_f32 v[14:15], v[14:15], v[14:15], s[8:9] op_sel_hi:[1,1,0]
	v_pk_fma_f32 v[44:45], v[44:45], v[44:45], s[8:9] op_sel_hi:[1,1,0]
	v_pk_mul_f32 v[16:17], v[32:33], v[16:17]
	v_pk_mul_f32 v[52:53], v[10:11], v[4:5]
	v_pk_mul_f32 v[54:55], v[12:13], v[6:7]
	v_pk_mul_f32 v[26:27], v[26:27], v[8:9]
	v_pk_mul_f32 v[28:29], v[28:29], v[0:1]
	v_pk_mul_f32 v[56:57], v[34:35], v[2:3]
	v_pk_mul_f32 v[58:59], v[36:37], v[14:15]
	v_pk_mul_f32 v[60:61], v[30:31], v[44:45]
	s_cmp_lt_u32 s33, 8
	s_cbranch_scc1 .Lprio_half
	s_setprio 0
.Lprio_half:
	ds_read_b128 v[0:3], v72 offset:12288
	ds_read_b128 v[4:7], v71 offset:42752
	ds_read_b128 v[8:11], v72 offset:13312
	ds_read_b128 v[12:15], v72 offset:14336
	ds_read_b128 v[34:37], v72 offset:15360
	ds_read_b128 v[44:47], v71 offset:42816
	v_cvt_pk_f16_f32 v30, v52, v53
	v_cvt_pk_f16_f32 v26, v26, v27
	v_cvt_pk_f16_f32 v31, v54, v55
	s_waitcnt lgkmcnt(4)
	v_mfma_f32_16x16x32_f16 v[48:51], v[0:3], v[22:25], v[4:7]
	v_cvt_pk_f16_f32 v32, v56, v57
	v_cvt_pk_f16_f32 v33, v58, v59
	v_cvt_pk_f16_f32 v27, v28, v29
	v_mfma_f32_16x16x32_f16 v[0:3], v[0:3], v[18:21], v[4:7]
	v_cvt_pk_f16_f32 v28, v16, v17
	v_cvt_pk_f16_f32 v29, v60, v61
	s_add_i32 s11, s9, s12
	s_waitcnt lgkmcnt(3)
	v_mfma_f32_16x16x32_f16 v[48:51], v[8:11], v[30:33], v[48:51]
	s_cmp_lt_i32 s11, 0x8000
	s_cselect_b32 s10, s11, s10
	s_ashr_i32 s11, s10, 31
	v_mfma_f32_16x16x32_f16 v[52:55], v[8:11], v[26:29], v[0:3]
	ds_read_b128 v[4:7], v72 offset:17408
	ds_read_b128 v[8:11], v71 offset:42880
	s_lshl_b64 s[10:11], s[10:11], 12
	s_add_u32 s10, s10, s36
	s_addc_u32 s11, s11, s37
	ds_read_b128 v[0:3], v72 offset:16384
	s_waitcnt lgkmcnt(3)
	v_mfma_f32_16x16x32_f16 v[56:59], v[12:15], v[22:25], v[44:47]
	v_exp_f32_e32 v106, v48
	v_exp_f32_e32 v107, v49
	v_exp_f32_e32 v110, v50
	v_mfma_f32_16x16x32_f16 v[12:15], v[12:15], v[18:21], v[44:47]
	v_exp_f32_e32 v111, v51
	v_exp_f32_e32 v114, v52
	v_exp_f32_e32 v115, v53
	v_mfma_f32_16x16x32_f16 v[44:47], v[34:37], v[30:33], v[56:59]
	v_mfma_f32_16x16x32_f16 v[56:59], v[34:37], v[26:29], v[12:15]
	ds_read_b128 v[34:37], v72 offset:19456
	ds_read_b128 v[60:63], v71 offset:42944
	s_nop 4
	v_exp_f32_e64 v108, v44 clamp
	ds_read_b128 v[12:15], v72 offset:18432
	s_waitcnt lgkmcnt(3)
	v_mfma_f32_16x16x32_f16 v[64:67], v[0:3], v[22:25], v[8:11]
	v_exp_f32_e64 v109, v45 clamp
	v_exp_f32_e64 v112, v46 clamp
	v_exp_f32_e64 v113, v47 clamp
	v_mfma_f32_16x16x32_f16 v[0:3], v[0:3], v[18:21], v[8:11]
	v_exp_f32_e64 v116, v56 clamp
	v_exp_f32_e64 v117, v57 clamp
	v_exp_f32_e64 v58, v58 clamp
	v_mfma_f32_16x16x32_f16 v[64:67], v[4:7], v[30:33], v[64:67]
	v_exp_f32_e64 v59, v59 clamp
	v_mfma_f32_16x16x32_f16 v[74:77], v[4:7], v[26:29], v[0:3]
	ds_read_b128 v[78:81], v72 offset:20480
	ds_read_b128 v[82:85], v72 offset:21504
	ds_read_b128 v[86:89], v71 offset:43008
	s_waitcnt lgkmcnt(3)
	v_mfma_f32_16x16x32_f16 v[6:9], v[12:15], v[22:25], v[60:63]
	v_mfma_f32_16x16x32_f16 v[60:63], v[12:15], v[18:21], v[60:63]
	global_load_dwordx4 v[10:13], v39, s[10:11] offset:16
	global_load_dwordx4 v[14:17], v39, s[10:11]
	global_load_dwordx4 v[2:5], v39, s[10:11] offset:2064
	v_mfma_f32_16x16x32_f16 v[90:93], v[34:37], v[30:33], v[6:9]
	v_mfma_f32_16x16x32_f16 v[60:63], v[34:37], v[26:29], v[60:63]
	s_nop 1
	global_load_dwordx4 v[6:9], v39, s[10:11] offset:2048
	ds_read_b128 v[94:97], v72 offset:22528
	ds_read_b128 v[98:101], v72 offset:23552
	ds_read_b128 v[102:105], v71 offset:43072
	s_waitcnt lgkmcnt(3)
	v_mfma_f32_16x16x32_f16 v[44:47], v[78:81], v[22:25], v[86:89]
	v_exp_f32_e32 v0, v64
	v_exp_f32_e32 v1, v65
	v_exp_f32_e32 v34, v66
	v_mfma_f32_16x16x32_f16 v[48:51], v[78:81], v[18:21], v[86:89]
	v_exp_f32_e32 v35, v67
	v_exp_f32_e32 v36, v74
	v_exp_f32_e32 v37, v75
	v_mfma_f32_16x16x32_f16 v[64:67], v[82:85], v[30:33], v[44:47]
	v_exp_f32_e32 v74, v54
	v_exp_f32_e32 v75, v55
	v_exp_f32_e32 v78, v92
	v_mfma_f32_16x16x32_f16 v[50:53], v[82:85], v[26:29], v[48:51]
	v_exp_f32_e32 v44, v76
	v_exp_f32_e32 v45, v77
	v_exp_f32_e32 v76, v90
	s_waitcnt lgkmcnt(0)
	v_mfma_f32_16x16x32_f16 v[46:49], v[94:97], v[22:25], v[102:105]
	v_exp_f32_e32 v77, v91
	v_exp_f32_e64 v64, v64 clamp
	v_exp_f32_e64 v65, v65 clamp
	v_mfma_f32_16x16x32_f16 v[54:57], v[94:97], v[18:21], v[102:105]
	v_exp_f32_e32 v79, v93
	v_exp_f32_e64 v66, v66 clamp
	v_exp_f32_e64 v67, v67 clamp
	v_mfma_f32_16x16x32_f16 v[46:49], v[98:101], v[30:33], v[46:49]
	v_exp_f32_e32 v60, v60
	v_exp_f32_e32 v61, v61
	v_exp_f32_e64 v50, v50 clamp
	v_mfma_f32_16x16x32_f16 v[54:57], v[98:101], v[26:29], v[54:57]
	v_exp_f32_e64 v51, v51 clamp
	s_nop 2
	v_exp_f32_e32 v46, v46
	v_exp_f32_e32 v47, v47
	v_exp_f32_e32 v48, v48
	v_exp_f32_e32 v49, v49
	v_exp_f32_e32 v54, v54
	v_exp_f32_e32 v55, v55
	v_exp_f32_e32 v62, v62
	v_exp_f32_e32 v63, v63
	v_exp_f32_e64 v52, v52 clamp
	v_exp_f32_e64 v53, v53 clamp
	v_exp_f32_e32 v56, v56
	v_exp_f32_e32 v57, v57
	v_pk_fma_f32 v[80:81], v[108:109], s[2:3], 1.0 op_sel_hi:[1,0,0]
	v_pk_fma_f32 v[82:83], v[112:113], s[2:3], 1.0 op_sel_hi:[1,0,0]
	v_pk_fma_f32 v[84:85], v[116:117], s[2:3], 1.0 op_sel_hi:[1,0,0]
	v_pk_fma_f32 v[58:59], v[58:59], s[2:3], 1.0 op_sel_hi:[1,0,0]
	v_pk_fma_f32 v[64:65], v[64:65], s[2:3], 1.0 op_sel_hi:[1,0,0]
	v_pk_fma_f32 v[66:67], v[66:67], s[2:3], 1.0 op_sel_hi:[1,0,0]
	v_pk_fma_f32 v[50:51], v[50:51], s[2:3], 1.0 op_sel_hi:[1,0,0]
	v_pk_fma_f32 v[52:53], v[52:53], s[2:3], 1.0 op_sel_hi:[1,0,0]
	v_pk_fma_f32 v[86:87], v[106:107], v[80:81], v[80:81]
	v_pk_fma_f32 v[88:89], v[110:111], v[82:83], v[82:83]
	v_pk_fma_f32 v[90:91], v[114:115], v[84:85], v[84:85]
	v_pk_fma_f32 v[74:75], v[74:75], v[58:59], v[58:59]
	v_pk_fma_f32 v[76:77], v[76:77], v[64:65], v[64:65]
	v_pk_fma_f32 v[78:79], v[78:79], v[66:67], v[66:67]
	v_pk_fma_f32 v[60:61], v[60:61], v[50:51], v[50:51]
	v_pk_fma_f32 v[62:63], v[62:63], v[52:53], v[52:53]
	v_pk_fma_f32 v[80:81], v[80:81], s[6:7], v[40:41] op_sel_hi:[1,0,0] neg_lo:[1,0,0] neg_hi:[1,0,0]
	v_pk_fma_f32 v[82:83], v[82:83], s[6:7], v[40:41] op_sel_hi:[1,0,0] neg_lo:[1,0,0] neg_hi:[1,0,0]
	v_pk_fma_f32 v[84:85], v[84:85], s[6:7], v[40:41] op_sel_hi:[1,0,0] neg_lo:[1,0,0] neg_hi:[1,0,0]
	v_pk_fma_f32 v[58:59], v[58:59], s[6:7], v[40:41] op_sel_hi:[1,0,0] neg_lo:[1,0,0] neg_hi:[1,0,0]
	v_pk_fma_f32 v[64:65], v[64:65], s[6:7], v[40:41] op_sel_hi:[1,0,0] neg_lo:[1,0,0] neg_hi:[1,0,0]
	v_pk_fma_f32 v[66:67], v[66:67], s[6:7], v[40:41] op_sel_hi:[1,0,0] neg_lo:[1,0,0] neg_hi:[1,0,0]
	v_pk_fma_f32 v[50:51], v[50:51], s[6:7], v[40:41] op_sel_hi:[1,0,0] neg_lo:[1,0,0] neg_hi:[1,0,0]
	v_pk_fma_f32 v[52:53], v[52:53], s[6:7], v[40:41] op_sel_hi:[1,0,0] neg_lo:[1,0,0] neg_hi:[1,0,0]
	v_pk_fma_f32 v[86:87], v[0:1], v[86:87], v[86:87]
	v_pk_fma_f32 v[88:89], v[34:35], v[88:89], v[88:89]
	v_pk_fma_f32 v[90:91], v[36:37], v[90:91], v[90:91]
	v_pk_fma_f32 v[74:75], v[44:45], v[74:75], v[74:75]
	v_pk_fma_f32 v[76:77], v[46:47], v[76:77], v[76:77]
	v_pk_fma_f32 v[78:79], v[48:49], v[78:79], v[78:79]
	v_pk_fma_f32 v[60:61], v[54:55], v[60:61], v[60:61]
	v_pk_fma_f32 v[62:63], v[56:57], v[62:63], v[62:63]
	v_rcp_f32_e64 v86, v86 clamp
	v_rcp_f32_e64 v87, v87 clamp
	v_rcp_f32_e64 v88, v88 clamp
	v_rcp_f32_e64 v89, v89 clamp
	v_rcp_f32_e64 v90, v90 clamp
	v_rcp_f32_e64 v91, v91 clamp
	v_rcp_f32_e64 v74, v74 clamp
	v_rcp_f32_e64 v75, v75 clamp
	v_rcp_f32_e64 v76, v76 clamp
	v_rcp_f32_e64 v77, v77 clamp
	v_rcp_f32_e64 v78, v78 clamp
	v_rcp_f32_e64 v79, v79 clamp
	v_rcp_f32_e64 v60, v60 clamp
	v_rcp_f32_e64 v61, v61 clamp
	v_rcp_f32_e64 v62, v62 clamp
	v_rcp_f32_e64 v63, v63 clamp
	v_pk_mul_f32 v[80:81], v[80:81], v[86:87]
	v_pk_mul_f32 v[82:83], v[82:83], v[88:89]
	v_pk_mul_f32 v[84:85], v[84:85], v[90:91]
	v_pk_mul_f32 v[58:59], v[58:59], v[74:75]
	v_pk_mul_f32 v[64:65], v[64:65], v[76:77]
	v_pk_mul_f32 v[66:67], v[66:67], v[78:79]
	v_pk_mul_f32 v[50:51], v[50:51], v[60:61]
	v_pk_mul_f32 v[60:61], v[52:53], v[62:63]
	v_pk_fma_f32 v[0:1], v[0:1], v[80:81], v[80:81]
	v_pk_fma_f32 v[34:35], v[34:35], v[82:83], v[82:83]
	v_pk_fma_f32 v[36:37], v[36:37], v[84:85], v[84:85]
	v_pk_fma_f32 v[44:45], v[44:45], v[58:59], v[58:59]
	v_pk_fma_f32 v[46:47], v[46:47], v[64:65], v[64:65]
	v_pk_fma_f32 v[48:49], v[48:49], v[66:67], v[66:67]
	v_pk_fma_f32 v[52:53], v[54:55], v[50:51], v[50:51]
	v_pk_fma_f32 v[54:55], v[56:57], v[60:61], v[60:61]
	s_nop 0
	v_pk_fma_f32 v[0:1], v[0:1], v[0:1], s[4:5] neg_lo:[1,0,0] neg_hi:[1,0,0] clamp
	v_pk_fma_f32 v[34:35], v[34:35], v[34:35], s[4:5] neg_lo:[1,0,0] neg_hi:[1,0,0] clamp
	v_pk_fma_f32 v[36:37], v[36:37], v[36:37], s[4:5] neg_lo:[1,0,0] neg_hi:[1,0,0] clamp
	v_pk_fma_f32 v[44:45], v[44:45], v[44:45], s[4:5] neg_lo:[1,0,0] neg_hi:[1,0,0] clamp
	v_pk_fma_f32 v[46:47], v[46:47], v[46:47], s[4:5] neg_lo:[1,0,0] neg_hi:[1,0,0] clamp
	v_pk_fma_f32 v[48:49], v[48:49], v[48:49], s[4:5] neg_lo:[1,0,0] neg_hi:[1,0,0] clamp
	v_pk_fma_f32 v[52:53], v[52:53], v[52:53], s[4:5] neg_lo:[1,0,0] neg_hi:[1,0,0] clamp
	s_nop 0
	v_pk_fma_f32 v[54:55], v[54:55], v[54:55], s[4:5] neg_lo:[1,0,0] neg_hi:[1,0,0] clamp
	s_nop 0
	v_pk_fma_f32 v[0:1], v[0:1], v[0:1], s[8:9] op_sel_hi:[1,1,0]
	v_pk_fma_f32 v[56:57], v[34:35], v[34:35], s[8:9] op_sel_hi:[1,1,0]
	v_pk_fma_f32 v[36:37], v[36:37], v[36:37], s[8:9] op_sel_hi:[1,1,0]
	v_pk_fma_f32 v[44:45], v[44:45], v[44:45], s[8:9] op_sel_hi:[1,1,0]
	v_pk_fma_f32 v[46:47], v[46:47], v[46:47], s[8:9] op_sel_hi:[1,1,0]
	v_pk_fma_f32 v[48:49], v[48:49], v[48:49], s[8:9] op_sel_hi:[1,1,0]
	v_pk_fma_f32 v[62:63], v[52:53], v[52:53], s[8:9] op_sel_hi:[1,1,0]
	v_pk_fma_f32 v[74:75], v[54:55], v[54:55], s[8:9] op_sel_hi:[1,1,0]
	v_pk_mul_f32 v[34:35], v[80:81], v[0:1]
	v_pk_mul_f32 v[56:57], v[82:83], v[56:57]
	v_pk_mul_f32 v[36:37], v[84:85], v[36:37]
	v_pk_mul_f32 v[52:53], v[58:59], v[44:45]
	v_pk_mul_f32 v[54:55], v[64:65], v[46:47]
	v_pk_mul_f32 v[0:1], v[66:67], v[48:49]
	v_pk_mul_f32 v[46:47], v[62:63], v[50:51]
	v_pk_mul_f32 v[44:45], v[60:61], v[74:75]
	ds_read_b128 v[48:51], v72 offset:24576
	ds_read_b128 v[58:61], v71 offset:43136
	ds_read_b128 v[62:65], v72 offset:25600
	ds_read_b128 v[74:77], v72 offset:26624
	ds_read_b128 v[78:81], v72 offset:27648
	ds_read_b128 v[82:85], v71 offset:43200
	v_cvt_pk_f16_f32 v34, v34, v35
	v_cvt_pk_f16_f32 v35, v56, v57
	s_waitcnt lgkmcnt(4)
	v_mfma_f32_16x16x32_f16 v[86:89], v[48:51], v[22:25], v[58:61]
	v_mfma_f32_16x16x32_f16 v[48:51], v[48:51], v[18:21], v[58:61]
	s_waitcnt lgkmcnt(3)
	v_mfma_f32_16x16x32_f16 v[58:61], v[62:65], v[30:33], v[86:89]
	v_mfma_f32_16x16x32_f16 v[86:89], v[62:65], v[26:29], v[48:51]
	ds_read_b128 v[62:65], v72 offset:29696
	ds_read_b128 v[90:93], v71 offset:43264
	s_nop 2
	ds_read_b128 v[48:51], v72 offset:28672
	s_waitcnt lgkmcnt(3)
	v_mfma_f32_16x16x32_f16 v[94:97], v[74:77], v[22:25], v[82:85]
	v_exp_f32_e32 v120, v86
	v_exp_f32_e32 v121, v87
	v_exp_f32_e32 v122, v88
	v_mfma_f32_16x16x32_f16 v[74:77], v[74:77], v[18:21], v[82:85]
	v_exp_f32_e32 v123, v89
	v_mfma_f32_16x16x32_f16 v[82:85], v[78:81], v[30:33], v[94:97]
	v_mfma_f32_16x16x32_f16 v[74:77], v[78:81], v[26:29], v[74:77]
	ds_read_b128 v[78:81], v72 offset:30720
	s_nop 0
	ds_read_b128 v[94:97], v72 offset:31744
	ds_read_b128 v[98:101], v71 offset:43328
	s_waitcnt lgkmcnt(3)
	v_mfma_f32_16x16x32_f16 v[102:105], v[48:51], v[22:25], v[90:93]
	s_nop 0
	v_exp_f32_e64 v66, v82 clamp
	v_exp_f32_e64 v67, v83 clamp
	v_exp_f32_e64 v118, v84 clamp
	v_mfma_f32_16x16x32_f16 v[48:51], v[48:51], v[18:21], v[90:93]
	v_exp_f32_e64 v119, v85 clamp
	v_exp_f32_e64 v124, v74 clamp
	v_exp_f32_e64 v125, v75 clamp
	v_mfma_f32_16x16x32_f16 v[90:93], v[62:65], v[30:33], v[102:105]
	v_exp_f32_e64 v126, v76 clamp
	v_exp_f32_e64 v127, v77 clamp
	v_mfma_f32_16x16x32_f16 v[102:105], v[62:65], v[26:29], v[48:51]
	ds_read_b128 v[106:109], v72 offset:32768
	ds_read_b128 v[110:113], v72 offset:33792
	v_exp_f32_e32 v62, v58
	v_exp_f32_e32 v63, v59
	v_exp_f32_e32 v64, v60
	v_exp_f32_e32 v65, v61
	ds_read_b128 v[114:117], v71 offset:43392
	s_waitcnt lgkmcnt(3)
	v_mfma_f32_16x16x32_f16 v[58:61], v[78:81], v[22:25], v[98:101]
	v_exp_f32_e32 v48, v90
	v_exp_f32_e32 v49, v91
	v_exp_f32_e32 v50, v92
	v_mfma_f32_16x16x32_f16 v[78:81], v[78:81], v[18:21], v[98:101]
	v_exp_f32_e32 v51, v93
	v_mfma_f32_16x16x32_f16 v[82:85], v[94:97], v[30:33], v[58:61]
	v_mfma_f32_16x16x32_f16 v[78:81], v[94:97], v[26:29], v[78:81]
	ds_read_b128 v[86:89], v72 offset:34816
	ds_read_b128 v[90:93], v72 offset:35840
	ds_read_b128 v[94:97], v71 offset:43456
	s_waitcnt lgkmcnt(3)
	v_mfma_f32_16x16x32_f16 v[74:77], v[106:109], v[22:25], v[114:117]
	v_exp_f32_e32 v58, v102
	v_exp_f32_e32 v59, v103
	v_exp_f32_e32 v60, v104
	v_mfma_f32_16x16x32_f16 v[98:101], v[106:109], v[18:21], v[114:117]
	v_exp_f32_e32 v61, v105
	v_exp_f32_e32 v102, v82
	v_exp_f32_e32 v103, v83
	v_exp_f32_e32 v104, v84
	v_exp_f32_e32 v105, v85
	v_mfma_f32_16x16x32_f16 v[74:77], v[110:113], v[30:33], v[74:77]
	v_mfma_f32_16x16x32_f16 v[82:85], v[110:113], v[26:29], v[98:101]
	s_waitcnt lgkmcnt(0)
	v_mfma_f32_16x16x32_f16 v[18:21], v[86:89], v[18:21], v[94:97]
	s_nop 4
	v_exp_f32_e64 v106, v74 clamp
	v_exp_f32_e64 v107, v75 clamp
	v_exp_f32_e64 v108, v76 clamp
	v_exp_f32_e64 v109, v77 clamp
	v_mfma_f32_16x16x32_f16 v[74:77], v[86:89], v[22:25], v[94:97]
	v_cvt_pk_f16_f32 v22, v36, v37
	v_cvt_pk_f16_f32 v23, v52, v53
	v_cvt_pk_f16_f32 v36, v54, v55
	v_mfma_f32_16x16x32_f16 v[18:21], v[90:93], v[26:29], v[18:21]
	v_exp_f32_e32 v52, v78
	v_exp_f32_e32 v53, v79
	v_exp_f32_e64 v54, v82 clamp
	v_mfma_f32_16x16x32_f16 v[30:33], v[90:93], v[30:33], v[74:77]
	v_exp_f32_e64 v55, v83 clamp
	s_nop 2
	v_exp_f32_e32 v18, v18
	v_exp_f32_e32 v19, v19
	v_exp_f32_e32 v26, v80
	v_exp_f32_e32 v27, v81
	v_exp_f32_e32 v30, v30
	v_exp_f32_e32 v31, v31
	v_exp_f32_e32 v32, v32
	v_exp_f32_e32 v33, v33
	v_exp_f32_e64 v28, v84 clamp
	v_exp_f32_e64 v29, v85 clamp
	v_exp_f32_e32 v20, v20
	v_cvt_pk_f16_f32 v24, v46, v47
	v_cvt_pk_f16_f32 v37, v0, v1
	v_cvt_pk_f16_f32 v25, v44, v45
	v_exp_f32_e32 v21, v21
	v_pk_fma_f32 v[0:1], v[66:67], s[2:3], 1.0 op_sel_hi:[1,0,0]
	v_pk_fma_f32 v[44:45], v[118:119], s[2:3], 1.0 op_sel_hi:[1,0,0]
	v_pk_fma_f32 v[46:47], v[124:125], s[2:3], 1.0 op_sel_hi:[1,0,0]
	v_pk_fma_f32 v[56:57], v[126:127], s[2:3], 1.0 op_sel_hi:[1,0,0]
	v_pk_fma_f32 v[66:67], v[106:107], s[2:3], 1.0 op_sel_hi:[1,0,0]
	v_pk_fma_f32 v[74:75], v[108:109], s[2:3], 1.0 op_sel_hi:[1,0,0]
	v_pk_fma_f32 v[54:55], v[54:55], s[2:3], 1.0 op_sel_hi:[1,0,0]
	v_pk_fma_f32 v[28:29], v[28:29], s[2:3], 1.0 op_sel_hi:[1,0,0]
	v_pk_fma_f32 v[62:63], v[62:63], v[0:1], v[0:1]
	v_pk_fma_f32 v[64:65], v[64:65], v[44:45], v[44:45]
	v_pk_fma_f32 v[76:77], v[120:121], v[46:47], v[46:47]
	v_pk_fma_f32 v[78:79], v[122:123], v[56:57], v[56:57]
	v_pk_fma_f32 v[80:81], v[102:103], v[66:67], v[66:67]
	v_pk_fma_f32 v[82:83], v[104:105], v[74:75], v[74:75]
	v_pk_fma_f32 v[52:53], v[52:53], v[54:55], v[54:55]
	v_pk_fma_f32 v[26:27], v[26:27], v[28:29], v[28:29]
	v_pk_fma_f32 v[0:1], v[0:1], s[6:7], v[40:41] op_sel_hi:[1,0,0] neg_lo:[1,0,0] neg_hi:[1,0,0]
	v_pk_fma_f32 v[44:45], v[44:45], s[6:7], v[40:41] op_sel_hi:[1,0,0] neg_lo:[1,0,0] neg_hi:[1,0,0]
	v_pk_fma_f32 v[46:47], v[46:47], s[6:7], v[40:41] op_sel_hi:[1,0,0] neg_lo:[1,0,0] neg_hi:[1,0,0]
	v_pk_fma_f32 v[56:57], v[56:57], s[6:7], v[40:41] op_sel_hi:[1,0,0] neg_lo:[1,0,0] neg_hi:[1,0,0]
	v_pk_fma_f32 v[66:67], v[66:67], s[6:7], v[40:41] op_sel_hi:[1,0,0] neg_lo:[1,0,0] neg_hi:[1,0,0]
	v_pk_fma_f32 v[74:75], v[74:75], s[6:7], v[40:41] op_sel_hi:[1,0,0] neg_lo:[1,0,0] neg_hi:[1,0,0]
	v_pk_fma_f32 v[54:55], v[54:55], s[6:7], v[40:41] op_sel_hi:[1,0,0] neg_lo:[1,0,0] neg_hi:[1,0,0]
	v_pk_fma_f32 v[28:29], v[28:29], s[6:7], v[40:41] op_sel_hi:[1,0,0] neg_lo:[1,0,0] neg_hi:[1,0,0]
	v_pk_fma_f32 v[62:63], v[48:49], v[62:63], v[62:63]
	v_pk_fma_f32 v[64:65], v[50:51], v[64:65], v[64:65]
	v_pk_fma_f32 v[76:77], v[58:59], v[76:77], v[76:77]
	v_pk_fma_f32 v[78:79], v[60:61], v[78:79], v[78:79]
	v_pk_fma_f32 v[80:81], v[30:31], v[80:81], v[80:81]
	v_pk_fma_f32 v[82:83], v[32:33], v[82:83], v[82:83]
	v_pk_fma_f32 v[52:53], v[18:19], v[52:53], v[52:53]
	v_pk_fma_f32 v[26:27], v[20:21], v[26:27], v[26:27]
	v_rcp_f32_e64 v62, v62 clamp
	v_rcp_f32_e64 v63, v63 clamp
	v_rcp_f32_e64 v64, v64 clamp
	v_rcp_f32_e64 v65, v65 clamp
	v_rcp_f32_e64 v76, v76 clamp
	v_rcp_f32_e64 v77, v77 clamp
	v_rcp_f32_e64 v78, v78 clamp
	v_rcp_f32_e64 v79, v79 clamp
	v_rcp_f32_e64 v80, v80 clamp
	v_rcp_f32_e64 v81, v81 clamp
	v_rcp_f32_e64 v82, v82 clamp
	v_rcp_f32_e64 v83, v83 clamp
	v_rcp_f32_e64 v52, v52 clamp
	v_rcp_f32_e64 v53, v53 clamp
	v_rcp_f32_e64 v26, v26 clamp
	v_rcp_f32_e64 v27, v27 clamp
	v_pk_mul_f32 v[52:53], v[54:55], v[52:53]
	v_pk_mul_f32 v[0:1], v[0:1], v[62:63]
	v_pk_mul_f32 v[44:45], v[44:45], v[64:65]
	v_pk_mul_f32 v[46:47], v[46:47], v[76:77]
	v_pk_mul_f32 v[56:57], v[56:57], v[78:79]
	v_pk_mul_f32 v[62:63], v[66:67], v[80:81]
	v_pk_mul_f32 v[64:65], v[74:75], v[82:83]
	v_pk_mul_f32 v[26:27], v[28:29], v[26:27]
	v_pk_fma_f32 v[18:19], v[18:19], v[52:53], v[52:53]
	v_pk_fma_f32 v[28:29], v[48:49], v[0:1], v[0:1]
	v_pk_fma_f32 v[48:49], v[50:51], v[44:45], v[44:45]
	v_pk_fma_f32 v[50:51], v[58:59], v[46:47], v[46:47]
	v_pk_fma_f32 v[54:55], v[60:61], v[56:57], v[56:57]
	v_pk_fma_f32 v[30:31], v[30:31], v[62:63], v[62:63]
	v_pk_fma_f32 v[32:33], v[32:33], v[64:65], v[64:65]
	v_pk_fma_f32 v[20:21], v[20:21], v[26:27], v[26:27]
	s_nop 0
	v_pk_fma_f32 v[28:29], v[28:29], v[28:29], s[4:5] neg_lo:[1,0,0] neg_hi:[1,0,0] clamp
	v_pk_fma_f32 v[48:49], v[48:49], v[48:49], s[4:5] neg_lo:[1,0,0] neg_hi:[1,0,0] clamp
	v_pk_fma_f32 v[50:51], v[50:51], v[50:51], s[4:5] neg_lo:[1,0,0] neg_hi:[1,0,0] clamp
	v_pk_fma_f32 v[54:55], v[54:55], v[54:55], s[4:5] neg_lo:[1,0,0] neg_hi:[1,0,0] clamp
	v_pk_fma_f32 v[30:31], v[30:31], v[30:31], s[4:5] neg_lo:[1,0,0] neg_hi:[1,0,0] clamp
	v_pk_fma_f32 v[32:33], v[32:33], v[32:33], s[4:5] neg_lo:[1,0,0] neg_hi:[1,0,0] clamp
	v_pk_fma_f32 v[18:19], v[18:19], v[18:19], s[4:5] neg_lo:[1,0,0] neg_hi:[1,0,0] clamp
	s_nop 0
	v_pk_fma_f32 v[20:21], v[20:21], v[20:21], s[4:5] neg_lo:[1,0,0] neg_hi:[1,0,0] clamp
	s_nop 0
	v_pk_fma_f32 v[28:29], v[28:29], v[28:29], s[8:9] op_sel_hi:[1,1,0]
	v_pk_fma_f32 v[48:49], v[48:49], v[48:49], s[8:9] op_sel_hi:[1,1,0]
	v_pk_fma_f32 v[50:51], v[50:51], v[50:51], s[8:9] op_sel_hi:[1,1,0]
	v_pk_fma_f32 v[54:55], v[54:55], v[54:55], s[8:9] op_sel_hi:[1,1,0]
	v_pk_fma_f32 v[30:31], v[30:31], v[30:31], s[8:9] op_sel_hi:[1,1,0]
	v_pk_fma_f32 v[32:33], v[32:33], v[32:33], s[8:9] op_sel_hi:[1,1,0]
	v_pk_fma_f32 v[18:19], v[18:19], v[18:19], s[8:9] op_sel_hi:[1,1,0]
	v_pk_fma_f32 v[20:21], v[20:21], v[20:21], s[8:9] op_sel_hi:[1,1,0]
	v_pk_mul_f32 v[0:1], v[0:1], v[28:29]
	v_pk_mul_f32 v[58:59], v[44:45], v[48:49]
	v_pk_mul_f32 v[60:61], v[46:47], v[50:51]
	v_pk_mul_f32 v[54:55], v[56:57], v[54:55]
	v_pk_mul_f32 v[62:63], v[62:63], v[30:31]
	v_pk_mul_f32 v[64:65], v[64:65], v[32:33]
	v_pk_mul_f32 v[66:67], v[18:19], v[52:53]
	v_pk_mul_f32 v[74:75], v[26:27], v[20:21]
	ds_read_b128 v[18:21], v72 offset:36864
	ds_read_b128 v[30:33], v72 offset:37888
	ds_read_b128 v[26:29], v71 offset:43520
	v_cvt_pk_f16_f32 v56, v60, v61
	v_cvt_pk_f16_f32 v57, v54, v55
	v_cvt_pk_f16_f32 v54, v62, v63
	ds_read_b128 v[60:63], v71 offset:43584
	v_cvt_pk_f16_f32 v52, v0, v1
	v_cvt_pk_f16_f32 v53, v58, v59
	s_waitcnt lgkmcnt(1)
	v_mfma_f32_16x16x32_f16 v[48:51], v[18:21], v[34:37], v[26:29]
	v_cvt_pk_f16_f32 v55, v64, v65
	v_cvt_pk_f16_f32 v58, v66, v67
	v_cvt_pk_f16_f32 v59, v74, v75
	v_mfma_f32_16x16x32_f16 v[18:21], v[18:21], v[22:25], v[26:29]
	ds_read_b128 v[44:47], v72 offset:40960
	s_add_i32 s12, s12, s3
	s_add_i32 s10, s20, s12
	v_mfma_f32_16x16x32_f16 v[26:29], v[30:33], v[52:55], v[48:51]
	s_cmp_lt_i32 s10, 0x8000
	v_add_u32_e32 v38, s7, v38
	s_nop 0
	ds_read_b128 v[48:51], v72 offset:38912
	v_mfma_f32_16x16x32_f16 v[18:21], v[30:33], v[56:59], v[18:21]
	ds_read_b128 v[30:33], v72 offset:39936
	s_nop 1
	v_cvt_pk_f16_f32 v1, v28, v29
	v_cvt_pk_f16_f32 v0, v26, v27
	s_waitcnt lgkmcnt(1)
	v_mfma_f32_16x16x32_f16 v[34:37], v[48:51], v[34:37], v[60:63]
	v_pk_max_f16 v27, v1, 0
	v_cvt_pk_f16_f32 v1, v20, v21
	v_pk_max_f16 v26, v0, 0
	v_mfma_f32_16x16x32_f16 v[20:23], v[48:51], v[22:25], v[60:63]
	v_cvt_pk_f16_f32 v0, v18, v19
	v_pk_max_f16 v18, v0, 0
	v_pk_max_f16 v19, v1, 0
	s_waitcnt lgkmcnt(0)
	v_mfma_f32_16x16x32_f16 v[34:37], v[30:33], v[52:55], v[34:37]
	v_mfma_f32_16x16x32_f16 v[20:23], v[30:33], v[56:59], v[20:23]
	s_nop 6
	v_cvt_pk_f16_f32 v0, v34, v35
	v_cvt_pk_f16_f32 v1, v36, v37
	v_pk_max_f16 v28, v0, 0
	v_pk_max_f16 v29, v1, 0
	v_cvt_pk_f16_f32 v0, v20, v21
	v_cvt_pk_f16_f32 v1, v22, v23
	v_pk_max_f16 v20, v0, 0
	v_pk_max_f16 v21, v1, 0
	v_mfma_f32_16x16x32_f16 v[24:27], v[44:47], v[26:29], 0
	s_nop 0
	v_mfma_f32_16x16x32_f16 v[18:21], v[44:47], v[18:21], 0
	s_nop 7
	v_cndmask_b32_e64 v18, v24, v18, s[0:1]
	s_cbranch_scc0 .LBB0_37
.LBB0_35:
	s_setprio 3
	s_cmp_lt_u32 s33, 5
	s_cbranch_scc1 .Lprio_done
	s_setprio 2
	s_cmp_lt_u32 s33, 6
	s_cbranch_scc1 .Lprio_done
	s_setprio 1
	s_cmp_lt_u32 s33, 8
	s_cbranch_scc1 .Lprio_done
	s_setprio 0
